# MoE down-projection epilogues: row-piece stores issued after the next piece's lane permutes (lgkmcnt(4)) where registers allow
# baseline (speedup 1.0000x reference)
.LBB0_1174:
	v_cvt_pk_bf16_f32 v142, v142, v143
	v_cvt_pk_bf16_f32 v143, v144, v145
	s_lshl_b32 s12, s78, 8
	v_lshl_add_u32 v154, s77, 8, v165
	v_cvt_pk_bf16_f32 v138, v138, v139
	v_cvt_pk_bf16_f32 v139, v140, v141
	ds_bpermute_b32 v140, v164, v142
	ds_bpermute_b32 v141, v164, v143
	ds_bpermute_b32 v142, v164, v138
	ds_bpermute_b32 v143, v164, v139
	s_and_b32 s12, s12, 0x300
	v_ashrrev_i32_e32 v155, 31, v154
	v_or_b32_e32 v146, s12, v166
	v_lshlrev_b64 v[138:139], 11, v[154:155]
	v_lshl_add_u64 v[138:139], s[18:19], 0, v[138:139]
	v_lshlrev_b32_e32 v146, 1, v146
	v_lshl_add_u64 v[138:139], v[138:139], 0, v[146:147]
	v_cvt_pk_bf16_f32 v134, v134, v135
	v_cvt_pk_bf16_f32 v135, v136, v137
	v_cvt_pk_bf16_f32 v136, v130, v131
	v_cvt_pk_bf16_f32 v133, v132, v133
	ds_bpermute_b32 v130, v164, v134
	ds_bpermute_b32 v131, v164, v135
	ds_bpermute_b32 v132, v164, v136
	ds_bpermute_b32 v133, v164, v133
	s_waitcnt lgkmcnt(4)
	global_store_dwordx4 v[138:139], v[140:143], off
	s_waitcnt lgkmcnt(0)
	global_store_dwordx4 v[138:139], v[130:133], off offset:256
	v_cvt_pk_bf16_f32 v126, v126, v127
	v_cvt_pk_bf16_f32 v127, v128, v129
	v_cvt_pk_bf16_f32 v128, v122, v123
	v_cvt_pk_bf16_f32 v125, v124, v125
	s_nop 1
	v_or_b32_e32 v130, 16, v154
	ds_bpermute_b32 v122, v164, v126
	ds_bpermute_b32 v123, v164, v127
	ds_bpermute_b32 v124, v164, v128
	ds_bpermute_b32 v125, v164, v125
	v_ashrrev_i32_e32 v131, 31, v130
	v_lshlrev_b64 v[126:127], 11, v[130:131]
	v_lshl_add_u64 v[126:127], s[18:19], 0, v[126:127]
	v_lshl_add_u64 v[126:127], v[126:127], 0, v[146:147]
	v_cvt_pk_bf16_f32 v118, v118, v119
	v_cvt_pk_bf16_f32 v119, v120, v121
	v_cvt_pk_bf16_f32 v120, v114, v115
	v_cvt_pk_bf16_f32 v117, v116, v117
	ds_bpermute_b32 v114, v164, v118
	ds_bpermute_b32 v115, v164, v119
	ds_bpermute_b32 v116, v164, v120
	ds_bpermute_b32 v117, v164, v117
	s_waitcnt lgkmcnt(4)
	global_store_dwordx4 v[126:127], v[122:125], off
	s_waitcnt lgkmcnt(0)
	global_store_dwordx4 v[126:127], v[114:117], off offset:256
	v_cvt_pk_bf16_f32 v110, v110, v111
	v_cvt_pk_bf16_f32 v111, v112, v113
	v_cvt_pk_bf16_f32 v112, v106, v107
	v_cvt_pk_bf16_f32 v109, v108, v109
	s_nop 1
	v_or_b32_e32 v114, 32, v154
	ds_bpermute_b32 v106, v164, v110
	ds_bpermute_b32 v107, v164, v111
	ds_bpermute_b32 v108, v164, v112
	ds_bpermute_b32 v109, v164, v109
	v_ashrrev_i32_e32 v115, 31, v114
	v_lshlrev_b64 v[110:111], 11, v[114:115]
	v_lshl_add_u64 v[110:111], s[18:19], 0, v[110:111]
	v_lshl_add_u64 v[110:111], v[110:111], 0, v[146:147]
	v_cvt_pk_bf16_f32 v102, v102, v103
	v_cvt_pk_bf16_f32 v103, v104, v105
	v_cvt_pk_bf16_f32 v104, v98, v99
	v_cvt_pk_bf16_f32 v101, v100, v101
	ds_bpermute_b32 v98, v164, v102
	ds_bpermute_b32 v99, v164, v103
	ds_bpermute_b32 v100, v164, v104
	ds_bpermute_b32 v101, v164, v101
	s_waitcnt lgkmcnt(4)
	global_store_dwordx4 v[110:111], v[106:109], off
	s_waitcnt lgkmcnt(0)
	global_store_dwordx4 v[110:111], v[98:101], off offset:256
	v_cvt_pk_bf16_f32 v94, v94, v95
	v_cvt_pk_bf16_f32 v95, v96, v97
	v_cvt_pk_bf16_f32 v96, v90, v91
	v_cvt_pk_bf16_f32 v93, v92, v93
	s_nop 1
	v_or_b32_e32 v98, 48, v154
	ds_bpermute_b32 v90, v164, v94
	ds_bpermute_b32 v91, v164, v95
	ds_bpermute_b32 v92, v164, v96
	ds_bpermute_b32 v93, v164, v93
	v_ashrrev_i32_e32 v99, 31, v98
	v_lshlrev_b64 v[94:95], 11, v[98:99]
	v_lshl_add_u64 v[94:95], s[18:19], 0, v[94:95]
	v_lshl_add_u64 v[94:95], v[94:95], 0, v[146:147]
	v_cvt_pk_bf16_f32 v86, v86, v87
	v_cvt_pk_bf16_f32 v87, v88, v89
	v_cvt_pk_bf16_f32 v88, v82, v83
	v_cvt_pk_bf16_f32 v85, v84, v85
	ds_bpermute_b32 v82, v164, v86
	ds_bpermute_b32 v83, v164, v87
	ds_bpermute_b32 v84, v164, v88
	ds_bpermute_b32 v85, v164, v85
	s_waitcnt lgkmcnt(4)
	global_store_dwordx4 v[94:95], v[90:93], off
	v_cvt_pk_bf16_f32 v78, v78, v79
	v_cvt_pk_bf16_f32 v79, v80, v81
	v_cvt_pk_bf16_f32 v80, v74, v75
	v_cvt_pk_bf16_f32 v77, v76, v77
	ds_bpermute_b32 v74, v164, v78
	ds_bpermute_b32 v75, v164, v79
	ds_bpermute_b32 v76, v164, v80
	ds_bpermute_b32 v77, v164, v77
	s_waitcnt lgkmcnt(4)
	global_store_dwordx4 v[94:95], v[82:85], off offset:256
	v_add_co_u32_e32 v78, vcc, s62, v138
	s_nop 1
	v_addc_co_u32_e32 v79, vcc, 0, v139, vcc
	v_cvt_pk_bf16_f32 v70, v70, v71
	v_cvt_pk_bf16_f32 v71, v72, v73
	v_cvt_pk_bf16_f32 v72, v66, v67
	v_cvt_pk_bf16_f32 v69, v68, v69
	ds_bpermute_b32 v66, v164, v70
	ds_bpermute_b32 v67, v164, v71
	ds_bpermute_b32 v68, v164, v72
	ds_bpermute_b32 v69, v164, v69
	s_waitcnt lgkmcnt(4)
	global_store_dwordx4 v[78:79], v[74:77], off
	v_lshl_add_u64 v[70:71], v[138:139], 0, s[14:15]
	v_cvt_pk_bf16_f32 v62, v62, v63
	v_cvt_pk_bf16_f32 v63, v64, v65
	v_cvt_pk_bf16_f32 v64, v58, v59
	v_cvt_pk_bf16_f32 v61, v60, v61
	ds_bpermute_b32 v58, v164, v62
	ds_bpermute_b32 v59, v164, v63
	ds_bpermute_b32 v60, v164, v64
	ds_bpermute_b32 v61, v164, v61
	s_waitcnt lgkmcnt(4)
	global_store_dwordx4 v[70:71], v[66:69], off offset:256
	v_add_co_u32_e32 v62, vcc, s63, v138
	s_nop 1
	v_addc_co_u32_e32 v63, vcc, 0, v139, vcc
	v_cvt_pk_bf16_f32 v54, v54, v55
	v_cvt_pk_bf16_f32 v55, v56, v57
	v_cvt_pk_bf16_f32 v56, v50, v51
	v_cvt_pk_bf16_f32 v53, v52, v53
	ds_bpermute_b32 v50, v164, v54
	ds_bpermute_b32 v51, v164, v55
	ds_bpermute_b32 v52, v164, v56
	ds_bpermute_b32 v53, v164, v53
	s_waitcnt lgkmcnt(4)
	global_store_dwordx4 v[62:63], v[58:61], off
	v_lshl_add_u64 v[54:55], v[138:139], 0, s[26:27]
	v_cvt_pk_bf16_f32 v46, v46, v47
	v_cvt_pk_bf16_f32 v47, v48, v49
	v_cvt_pk_bf16_f32 v48, v38, v39
	v_cvt_pk_bf16_f32 v41, v40, v41
	ds_bpermute_b32 v38, v164, v46
	ds_bpermute_b32 v39, v164, v47
	ds_bpermute_b32 v40, v164, v48
	ds_bpermute_b32 v41, v164, v41
	s_waitcnt lgkmcnt(4)
	global_store_dwordx4 v[54:55], v[50:53], off offset:256
	v_add_co_u32_e32 v46, vcc, s64, v138
	s_nop 1
	v_addc_co_u32_e32 v47, vcc, 0, v139, vcc
	s_waitcnt lgkmcnt(0)
	global_store_dwordx4 v[46:47], v[38:41], off
	s_nop 1
	v_cvt_pk_bf16_f32 v38, v42, v43
	v_cvt_pk_bf16_f32 v39, v44, v45
	v_cvt_pk_bf16_f32 v40, v34, v35
	v_cvt_pk_bf16_f32 v37, v36, v37
	ds_bpermute_b32 v34, v164, v38
	ds_bpermute_b32 v35, v164, v39
	ds_bpermute_b32 v36, v164, v40
	ds_bpermute_b32 v37, v164, v37
	v_lshl_add_u64 v[38:39], v[138:139], 0, s[28:29]
	v_cvt_pk_bf16_f32 v26, v26, v27
	v_cvt_pk_bf16_f32 v27, v28, v29
	v_cvt_pk_bf16_f32 v28, v18, v19
	v_cvt_pk_bf16_f32 v21, v20, v21
	ds_bpermute_b32 v18, v164, v26
	ds_bpermute_b32 v19, v164, v27
	ds_bpermute_b32 v20, v164, v28
	ds_bpermute_b32 v21, v164, v21
	s_waitcnt lgkmcnt(4)
	global_store_dwordx4 v[38:39], v[34:37], off offset:256
	v_add_co_u32_e32 v26, vcc, s65, v138
	s_nop 1
	v_addc_co_u32_e32 v27, vcc, 0, v139, vcc
	s_waitcnt lgkmcnt(0)
	global_store_dwordx4 v[26:27], v[18:21], off
	s_and_b64 vcc, exec, s[0:1]
	s_mov_b64 s[0:1], -1
	v_cvt_pk_bf16_f32 v18, v30, v31
	v_cvt_pk_bf16_f32 v19, v32, v33
	v_cvt_pk_bf16_f32 v20, v22, v23
	v_cvt_pk_bf16_f32 v21, v24, v25
	ds_bpermute_b32 v18, v164, v18
	ds_bpermute_b32 v19, v164, v19
	ds_bpermute_b32 v20, v164, v20
	ds_bpermute_b32 v21, v164, v21
	v_lshl_add_u64 v[22:23], v[138:139], 0, s[36:37]
	s_waitcnt lgkmcnt(0)
	global_store_dwordx4 v[22:23], v[18:21], off offset:256
	s_cbranch_vccnz .LBB0_1160
	s_andn2_b64 vcc, exec, s[16:17]
	s_cbranch_vccnz .LBB0_1159
	s_barrier
	s_branch .LBB0_1159

.LBB0_1330:
	v_cvt_pk_bf16_f32 v142, v142, v143
	v_cvt_pk_bf16_f32 v143, v144, v145
	s_lshl_b32 s10, s88, 8
	v_lshl_add_u32 v154, s87, 8, v165
	v_cvt_pk_bf16_f32 v138, v138, v139
	v_cvt_pk_bf16_f32 v139, v140, v141
	ds_bpermute_b32 v140, v164, v142
	ds_bpermute_b32 v141, v164, v143
	ds_bpermute_b32 v142, v164, v138
	ds_bpermute_b32 v143, v164, v139
	s_and_b32 s10, s10, 0x300
	v_ashrrev_i32_e32 v155, 31, v154
	v_or_b32_e32 v146, s10, v166
	v_lshlrev_b64 v[138:139], 11, v[154:155]
	v_lshl_add_u64 v[138:139], s[16:17], 0, v[138:139]
	v_lshlrev_b32_e32 v146, 1, v146
	v_lshl_add_u64 v[138:139], v[138:139], 0, v[146:147]
	v_cvt_pk_bf16_f32 v134, v134, v135
	v_cvt_pk_bf16_f32 v135, v136, v137
	v_cvt_pk_bf16_f32 v136, v130, v131
	v_cvt_pk_bf16_f32 v133, v132, v133
	ds_bpermute_b32 v130, v164, v134
	ds_bpermute_b32 v131, v164, v135
	ds_bpermute_b32 v132, v164, v136
	ds_bpermute_b32 v133, v164, v133
	s_waitcnt lgkmcnt(4)
	global_store_dwordx4 v[138:139], v[140:143], off
	s_mov_b32 s10, 0x10000
	v_cvt_pk_bf16_f32 v126, v126, v127
	v_cvt_pk_bf16_f32 v127, v128, v129
	v_cvt_pk_bf16_f32 v128, v122, v123
	v_cvt_pk_bf16_f32 v125, v124, v125
	ds_bpermute_b32 v122, v164, v126
	ds_bpermute_b32 v123, v164, v127
	ds_bpermute_b32 v124, v164, v128
	ds_bpermute_b32 v125, v164, v125
	s_waitcnt lgkmcnt(4)
	global_store_dwordx4 v[138:139], v[130:133], off offset:256
	v_add_co_u32_e32 v126, vcc, s64, v138
	s_nop 1
	v_addc_co_u32_e32 v127, vcc, 0, v139, vcc
	v_cvt_pk_bf16_f32 v118, v118, v119
	v_cvt_pk_bf16_f32 v119, v120, v121
	v_cvt_pk_bf16_f32 v120, v114, v115
	v_cvt_pk_bf16_f32 v117, v116, v117
	ds_bpermute_b32 v114, v164, v118
	ds_bpermute_b32 v115, v164, v119
	ds_bpermute_b32 v116, v164, v120
	ds_bpermute_b32 v117, v164, v117
	s_waitcnt lgkmcnt(4)
	global_store_dwordx4 v[126:127], v[122:125], off
	v_lshl_add_u64 v[118:119], v[138:139], 0, s[24:25]
	v_cvt_pk_bf16_f32 v110, v110, v111
	v_cvt_pk_bf16_f32 v111, v112, v113
	v_cvt_pk_bf16_f32 v112, v106, v107
	v_cvt_pk_bf16_f32 v109, v108, v109
	ds_bpermute_b32 v106, v164, v110
	ds_bpermute_b32 v107, v164, v111
	ds_bpermute_b32 v108, v164, v112
	ds_bpermute_b32 v109, v164, v109
	s_waitcnt lgkmcnt(4)
	global_store_dwordx4 v[118:119], v[114:117], off offset:256
	v_add_co_u32_e32 v110, vcc, s10, v138
	s_nop 1
	v_addc_co_u32_e32 v111, vcc, 0, v139, vcc
	v_cvt_pk_bf16_f32 v102, v102, v103
	v_cvt_pk_bf16_f32 v103, v104, v105
	v_cvt_pk_bf16_f32 v104, v98, v99
	v_cvt_pk_bf16_f32 v101, v100, v101
	ds_bpermute_b32 v98, v164, v102
	ds_bpermute_b32 v99, v164, v103
	ds_bpermute_b32 v100, v164, v104
	ds_bpermute_b32 v101, v164, v101
	s_waitcnt lgkmcnt(4)
	global_store_dwordx4 v[110:111], v[106:109], off
	v_lshl_add_u64 v[102:103], v[138:139], 0, s[26:27]
	v_cvt_pk_bf16_f32 v94, v94, v95
	v_cvt_pk_bf16_f32 v95, v96, v97
	v_cvt_pk_bf16_f32 v96, v90, v91
	v_cvt_pk_bf16_f32 v93, v92, v93
	ds_bpermute_b32 v90, v164, v94
	ds_bpermute_b32 v91, v164, v95
	ds_bpermute_b32 v92, v164, v96
	ds_bpermute_b32 v93, v164, v93
	s_waitcnt lgkmcnt(4)
	global_store_dwordx4 v[102:103], v[98:101], off offset:256
	v_add_co_u32_e32 v94, vcc, s63, v138
	s_nop 1
	v_addc_co_u32_e32 v95, vcc, 0, v139, vcc
	v_cvt_pk_bf16_f32 v86, v86, v87
	v_cvt_pk_bf16_f32 v87, v88, v89
	v_cvt_pk_bf16_f32 v88, v82, v83
	v_cvt_pk_bf16_f32 v85, v84, v85
	ds_bpermute_b32 v82, v164, v86
	ds_bpermute_b32 v83, v164, v87
	ds_bpermute_b32 v84, v164, v88
	ds_bpermute_b32 v85, v164, v85
	s_waitcnt lgkmcnt(4)
	global_store_dwordx4 v[94:95], v[90:93], off
	v_lshl_add_u64 v[86:87], v[138:139], 0, s[28:29]
	v_cvt_pk_bf16_f32 v78, v78, v79
	v_cvt_pk_bf16_f32 v79, v80, v81
	v_cvt_pk_bf16_f32 v80, v74, v75
	v_cvt_pk_bf16_f32 v77, v76, v77
	ds_bpermute_b32 v74, v164, v78
	ds_bpermute_b32 v75, v164, v79
	ds_bpermute_b32 v76, v164, v80
	ds_bpermute_b32 v77, v164, v77
	s_waitcnt lgkmcnt(4)
	global_store_dwordx4 v[86:87], v[82:85], off offset:256
	v_add_co_u32_e32 v78, vcc, s79, v138
	s_nop 1
	v_addc_co_u32_e32 v79, vcc, 0, v139, vcc
	v_cvt_pk_bf16_f32 v70, v70, v71
	v_cvt_pk_bf16_f32 v71, v72, v73
	v_cvt_pk_bf16_f32 v72, v66, v67
	v_cvt_pk_bf16_f32 v69, v68, v69
	ds_bpermute_b32 v66, v164, v70
	ds_bpermute_b32 v67, v164, v71
	ds_bpermute_b32 v68, v164, v72
	ds_bpermute_b32 v69, v164, v69
	s_waitcnt lgkmcnt(4)
	global_store_dwordx4 v[78:79], v[74:77], off
	v_lshl_add_u64 v[70:71], v[138:139], 0, s[12:13]
	v_cvt_pk_bf16_f32 v62, v62, v63
	v_cvt_pk_bf16_f32 v63, v64, v65
	v_cvt_pk_bf16_f32 v64, v58, v59
	v_cvt_pk_bf16_f32 v61, v60, v61
	ds_bpermute_b32 v58, v164, v62
	ds_bpermute_b32 v59, v164, v63
	ds_bpermute_b32 v60, v164, v64
	ds_bpermute_b32 v61, v164, v61
	s_waitcnt lgkmcnt(4)
	global_store_dwordx4 v[70:71], v[66:69], off offset:256
	v_add_co_u32_e32 v62, vcc, s80, v138
	s_nop 1
	v_addc_co_u32_e32 v63, vcc, 0, v139, vcc
	v_cvt_pk_bf16_f32 v54, v54, v55
	v_cvt_pk_bf16_f32 v55, v56, v57
	v_cvt_pk_bf16_f32 v56, v50, v51
	v_cvt_pk_bf16_f32 v53, v52, v53
	ds_bpermute_b32 v50, v164, v54
	ds_bpermute_b32 v51, v164, v55
	ds_bpermute_b32 v52, v164, v56
	ds_bpermute_b32 v53, v164, v53
	s_waitcnt lgkmcnt(4)
	global_store_dwordx4 v[62:63], v[58:61], off
	v_lshl_add_u64 v[54:55], v[138:139], 0, s[36:37]
	v_cvt_pk_bf16_f32 v46, v46, v47
	v_cvt_pk_bf16_f32 v47, v48, v49
	v_cvt_pk_bf16_f32 v48, v38, v39
	v_cvt_pk_bf16_f32 v41, v40, v41
	ds_bpermute_b32 v38, v164, v46
	ds_bpermute_b32 v39, v164, v47
	ds_bpermute_b32 v40, v164, v48
	ds_bpermute_b32 v41, v164, v41
	s_waitcnt lgkmcnt(4)
	global_store_dwordx4 v[54:55], v[50:53], off offset:256
	v_add_co_u32_e32 v46, vcc, s81, v138
	s_nop 1
	v_addc_co_u32_e32 v47, vcc, 0, v139, vcc
	s_waitcnt lgkmcnt(0)
	global_store_dwordx4 v[46:47], v[38:41], off
	s_nop 1
	v_cvt_pk_bf16_f32 v38, v42, v43
	v_cvt_pk_bf16_f32 v39, v44, v45
	v_cvt_pk_bf16_f32 v40, v34, v35
	v_cvt_pk_bf16_f32 v37, v36, v37
	ds_bpermute_b32 v34, v164, v38
	ds_bpermute_b32 v35, v164, v39
	ds_bpermute_b32 v36, v164, v40
	ds_bpermute_b32 v37, v164, v37
	v_lshl_add_u64 v[38:39], v[138:139], 0, s[38:39]
	v_cvt_pk_bf16_f32 v26, v26, v27
	v_cvt_pk_bf16_f32 v27, v28, v29
	v_cvt_pk_bf16_f32 v28, v18, v19
	v_cvt_pk_bf16_f32 v21, v20, v21
	ds_bpermute_b32 v18, v164, v26
	ds_bpermute_b32 v19, v164, v27
	ds_bpermute_b32 v20, v164, v28
	ds_bpermute_b32 v21, v164, v21
	s_waitcnt lgkmcnt(4)
	global_store_dwordx4 v[38:39], v[34:37], off offset:256
	v_add_co_u32_e32 v26, vcc, s82, v138
	s_nop 1
	v_addc_co_u32_e32 v27, vcc, 0, v139, vcc
	s_waitcnt lgkmcnt(0)
	global_store_dwordx4 v[26:27], v[18:21], off
	s_and_b64 vcc, exec, s[0:1]
	s_mov_b64 s[0:1], -1
	v_cvt_pk_bf16_f32 v18, v30, v31
	v_cvt_pk_bf16_f32 v19, v32, v33
	v_cvt_pk_bf16_f32 v20, v22, v23
	v_cvt_pk_bf16_f32 v21, v24, v25
	ds_bpermute_b32 v18, v164, v18
	ds_bpermute_b32 v19, v164, v19
	ds_bpermute_b32 v20, v164, v20
	ds_bpermute_b32 v21, v164, v21
	v_lshl_add_u64 v[22:23], v[138:139], 0, s[40:41]
	s_waitcnt lgkmcnt(0)
	global_store_dwordx4 v[22:23], v[18:21], off offset:256
	s_cbranch_vccnz .LBB0_1316
	s_andn2_b64 vcc, exec, s[14:15]
	s_cbranch_vccnz .LBB0_1315
	s_barrier
	s_branch .LBB0_1315
